# rwkv_pre S3: next diagonal block's coefficients prefetched column by column inside the solve (registers reused as each column retires); initial load only for the first block
# baseline (speedup 1.0000x reference)
.LBB0_623:
	s_cmpk_eq_i32 s11, 0x30c0
	s_cbranch_scc1 .Ls3_lastsolve
	v_fmac_f32_e32 v3, v228, v2
	s_nop 1
	v_pk_fma_f32 v[4:5], v[70:71], v[2:3], v[4:5] op_sel_hi:[1,0,1]
	v_pk_fma_f32 v[6:7], v[72:73], v[2:3], v[6:7] op_sel_hi:[1,0,1]
	v_pk_fma_f32 v[8:9], v[74:75], v[2:3], v[8:9] op_sel_hi:[1,0,1]
	v_pk_fma_f32 v[10:11], v[76:77], v[2:3], v[10:11] op_sel_hi:[1,0,1]
	v_pk_fma_f32 v[12:13], v[78:79], v[2:3], v[12:13] op_sel_hi:[1,0,1]
	v_pk_fma_f32 v[14:15], v[80:81], v[2:3], v[14:15] op_sel_hi:[1,0,1]
	v_pk_fma_f32 v[16:17], v[82:83], v[2:3], v[16:17] op_sel_hi:[1,0,1]
	ds_read_b32 v228, v181 offset:4164
	ds_read_b64 v[70:71], v181 offset:4168
	ds_read_b128 v[72:75], v181 offset:4176
	ds_read_b128 v[76:79], v181 offset:4192
	ds_read_b128 v[80:83], v181 offset:4208
	v_pk_fma_f32 v[4:5], v[84:85], v[2:3], v[4:5] op_sel:[0,1,0]
	v_pk_fma_f32 v[6:7], v[86:87], v[2:3], v[6:7] op_sel:[0,1,0]
	v_pk_fma_f32 v[8:9], v[88:89], v[2:3], v[8:9] op_sel:[0,1,0]
	v_pk_fma_f32 v[10:11], v[90:91], v[2:3], v[10:11] op_sel:[0,1,0]
	v_pk_fma_f32 v[12:13], v[92:93], v[2:3], v[12:13] op_sel:[0,1,0]
	v_pk_fma_f32 v[14:15], v[94:95], v[2:3], v[14:15] op_sel:[0,1,0]
	v_pk_fma_f32 v[16:17], v[96:97], v[2:3], v[16:17] op_sel:[0,1,0]
	ds_read_b64 v[84:85], v181 offset:4424
	ds_read_b128 v[86:89], v181 offset:4432
	ds_read_b128 v[90:93], v181 offset:4448
	ds_read_b128 v[94:97], v181 offset:4464
	v_fmac_f32_e32 v5, v230, v4
	s_nop 1
	v_pk_fma_f32 v[6:7], v[98:99], v[4:5], v[6:7] op_sel_hi:[1,0,1]
	v_pk_fma_f32 v[8:9], v[100:101], v[4:5], v[8:9] op_sel_hi:[1,0,1]
	v_pk_fma_f32 v[10:11], v[102:103], v[4:5], v[10:11] op_sel_hi:[1,0,1]
	v_pk_fma_f32 v[12:13], v[104:105], v[4:5], v[12:13] op_sel_hi:[1,0,1]
	v_pk_fma_f32 v[14:15], v[106:107], v[4:5], v[14:15] op_sel_hi:[1,0,1]
	v_pk_fma_f32 v[16:17], v[108:109], v[4:5], v[16:17] op_sel_hi:[1,0,1]
	ds_read_b32 v230, v181 offset:4684
	ds_read_b128 v[98:101], v181 offset:4688
	ds_read_b128 v[102:105], v181 offset:4704
	ds_read_b128 v[106:109], v181 offset:4720
	v_pk_fma_f32 v[6:7], v[110:111], v[4:5], v[6:7] op_sel:[0,1,0]
	v_pk_fma_f32 v[8:9], v[112:113], v[4:5], v[8:9] op_sel:[0,1,0]
	v_pk_fma_f32 v[10:11], v[114:115], v[4:5], v[10:11] op_sel:[0,1,0]
	v_pk_fma_f32 v[12:13], v[116:117], v[4:5], v[12:13] op_sel:[0,1,0]
	v_pk_fma_f32 v[14:15], v[118:119], v[4:5], v[14:15] op_sel:[0,1,0]
	v_pk_fma_f32 v[16:17], v[120:121], v[4:5], v[16:17] op_sel:[0,1,0]
	ds_read_b128 v[110:113], v181 offset:4944
	ds_read_b128 v[114:117], v181 offset:4960
	ds_read_b128 v[118:121], v181 offset:4976
	v_fmac_f32_e32 v7, v233, v6
	s_nop 1
	v_pk_fma_f32 v[8:9], v[122:123], v[6:7], v[8:9] op_sel_hi:[1,0,1]
	v_pk_fma_f32 v[10:11], v[124:125], v[6:7], v[10:11] op_sel_hi:[1,0,1]
	v_pk_fma_f32 v[12:13], v[126:127], v[6:7], v[12:13] op_sel_hi:[1,0,1]
	v_pk_fma_f32 v[14:15], v[128:129], v[6:7], v[14:15] op_sel_hi:[1,0,1]
	v_pk_fma_f32 v[16:17], v[130:131], v[6:7], v[16:17] op_sel_hi:[1,0,1]
	ds_read_b32 v233, v181 offset:5204
	ds_read_b64 v[122:123], v181 offset:5208
	ds_read_b128 v[124:127], v181 offset:5216
	ds_read_b128 v[128:131], v181 offset:5232
	v_pk_fma_f32 v[8:9], v[132:133], v[6:7], v[8:9] op_sel:[0,1,0]
	v_pk_fma_f32 v[10:11], v[134:135], v[6:7], v[10:11] op_sel:[0,1,0]
	v_pk_fma_f32 v[12:13], v[136:137], v[6:7], v[12:13] op_sel:[0,1,0]
	v_pk_fma_f32 v[14:15], v[138:139], v[6:7], v[14:15] op_sel:[0,1,0]
	v_pk_fma_f32 v[16:17], v[140:141], v[6:7], v[16:17] op_sel:[0,1,0]
	ds_read_b64 v[132:133], v181 offset:5464
	ds_read_b128 v[134:137], v181 offset:5472
	ds_read_b128 v[138:141], v181 offset:5488
	v_fmac_f32_e32 v9, v235, v8
	s_nop 1
	v_pk_fma_f32 v[10:11], v[142:143], v[8:9], v[10:11] op_sel_hi:[1,0,1]
	v_pk_fma_f32 v[12:13], v[144:145], v[8:9], v[12:13] op_sel_hi:[1,0,1]
	v_pk_fma_f32 v[14:15], v[146:147], v[8:9], v[14:15] op_sel_hi:[1,0,1]
	v_pk_fma_f32 v[16:17], v[148:149], v[8:9], v[16:17] op_sel_hi:[1,0,1]
	ds_read_b32 v235, v181 offset:5724
	ds_read_b128 v[142:145], v181 offset:5728
	ds_read_b128 v[146:149], v181 offset:5744
	v_pk_fma_f32 v[10:11], v[150:151], v[8:9], v[10:11] op_sel:[0,1,0]
	v_pk_fma_f32 v[12:13], v[152:153], v[8:9], v[12:13] op_sel:[0,1,0]
	v_pk_fma_f32 v[14:15], v[154:155], v[8:9], v[14:15] op_sel:[0,1,0]
	v_pk_fma_f32 v[16:17], v[156:157], v[8:9], v[16:17] op_sel:[0,1,0]
	ds_read_b128 v[150:153], v181 offset:5984
	ds_read_b128 v[154:157], v181 offset:6000
	v_fmac_f32_e32 v11, v236, v10
	s_nop 1
	v_pk_fma_f32 v[12:13], v[158:159], v[10:11], v[12:13] op_sel_hi:[1,0,1]
	v_pk_fma_f32 v[14:15], v[160:161], v[10:11], v[14:15] op_sel_hi:[1,0,1]
	v_pk_fma_f32 v[16:17], v[162:163], v[10:11], v[16:17] op_sel_hi:[1,0,1]
	ds_read_b32 v236, v181 offset:6244
	ds_read_b64 v[158:159], v181 offset:6248
	ds_read_b128 v[160:163], v181 offset:6256
	v_pk_fma_f32 v[12:13], v[164:165], v[10:11], v[12:13] op_sel:[0,1,0]
	v_pk_fma_f32 v[14:15], v[188:189], v[10:11], v[14:15] op_sel:[0,1,0]
	v_pk_fma_f32 v[16:17], v[190:191], v[10:11], v[16:17] op_sel:[0,1,0]
	ds_read_b64 v[164:165], v181 offset:6504
	ds_read_b128 v[188:191], v181 offset:6512
	v_fmac_f32_e32 v13, v237, v12
	s_nop 1
	v_pk_fma_f32 v[14:15], v[192:193], v[12:13], v[14:15] op_sel_hi:[1,0,1]
	v_pk_fma_f32 v[16:17], v[194:195], v[12:13], v[16:17] op_sel_hi:[1,0,1]
	ds_read_b32 v237, v181 offset:6764
	ds_read_b128 v[192:195], v181 offset:6768
	v_pk_fma_f32 v[14:15], v[196:197], v[12:13], v[14:15] op_sel:[0,1,0]
	v_pk_fma_f32 v[16:17], v[198:199], v[12:13], v[16:17] op_sel:[0,1,0]
	ds_read_b128 v[196:199], v181 offset:7024
	v_fmac_f32_e32 v15, v238, v14
	s_nop 1
	v_pk_fma_f32 v[16:17], v[200:201], v[14:15], v[16:17] op_sel_hi:[1,0,1]
	ds_read_b32 v238, v181 offset:7284
	ds_read_b64 v[200:201], v181 offset:7288
	v_pk_fma_f32 v[16:17], v[202:203], v[14:15], v[16:17] op_sel:[0,1,0]
	ds_read_b64 v[202:203], v181 offset:7544
	v_fmac_f32_e32 v17, v239, v16
	ds_read_b32 v239, v181 offset:7804
	s_nop 0
	v_cvt_pk_bf16_f32 v18, v2, v3
	v_cvt_pk_bf16_f32 v19, v4, v5
	v_cvt_pk_bf16_f32 v20, v6, v7
	v_cvt_pk_bf16_f32 v21, v8, v9
	v_cvt_pk_bf16_f32 v22, v10, v11
	v_cvt_pk_bf16_f32 v23, v12, v13
	v_cvt_pk_bf16_f32 v24, v14, v15
	v_cvt_pk_bf16_f32 v25, v16, v17
	ds_write_b128 v169, v[18:21]
	ds_write_b128 v169, v[22:25] offset:16
	s_branch .LBB0_624

.LBB0_634:
	s_or_b64 exec, exec, s[14:15]
	s_add_i32 s14, s11, 0
	s_add_i32 s15, s14, 0x1d400
	v_mov_b32_e32 v181, s15
	s_cmp_lg_u32 s11, 0
	s_cbranch_scc1 .Ls3_noload
	ds_read_b32 v228, v181 offset:4
	ds_read_b64 v[70:71], v181 offset:8
	ds_read_b128 v[72:75], v181 offset:16
	ds_read_b128 v[76:79], v181 offset:32
	ds_read_b128 v[80:83], v181 offset:48
	ds_read_b64 v[84:85], v181 offset:264
	ds_read_b128 v[86:89], v181 offset:272
	ds_read_b128 v[90:93], v181 offset:288
	ds_read_b128 v[94:97], v181 offset:304
	ds_read_b32 v230, v181 offset:524
	ds_read_b128 v[98:101], v181 offset:528
	ds_read_b128 v[102:105], v181 offset:544
	ds_read_b128 v[106:109], v181 offset:560
	ds_read_b128 v[110:113], v181 offset:784
	ds_read_b128 v[114:117], v181 offset:800
	ds_read_b128 v[118:121], v181 offset:816
	ds_read_b32 v233, v181 offset:1044
	ds_read_b64 v[122:123], v181 offset:1048
	ds_read_b128 v[124:127], v181 offset:1056
	ds_read_b128 v[128:131], v181 offset:1072
	ds_read_b64 v[132:133], v181 offset:1304
	ds_read_b128 v[134:137], v181 offset:1312
	ds_read_b128 v[138:141], v181 offset:1328
	ds_read_b32 v235, v181 offset:1564
	ds_read_b128 v[142:145], v181 offset:1568
	ds_read_b128 v[146:149], v181 offset:1584
	ds_read_b128 v[150:153], v181 offset:1824
	ds_read_b128 v[154:157], v181 offset:1840
	ds_read_b32 v236, v181 offset:2084
	ds_read_b64 v[158:159], v181 offset:2088
	ds_read_b128 v[160:163], v181 offset:2096
	ds_read_b64 v[164:165], v181 offset:2344
	ds_read_b128 v[188:191], v181 offset:2352
	ds_read_b32 v237, v181 offset:2604
	ds_read_b128 v[192:195], v181 offset:2608
	ds_read_b128 v[196:199], v181 offset:2864
	ds_read_b32 v238, v181 offset:3124
	ds_read_b64 v[200:201], v181 offset:3128
	ds_read_b64 v[202:203], v181 offset:3384
	ds_read_b32 v239, v181 offset:3644
.Ls3_noload:
.LBB0_635:
	s_or_b64 exec, exec, s[12:13]
	s_waitcnt lgkmcnt(0)
	s_barrier
	s_and_saveexec_b64 s[12:13], s[0:1]
	s_cbranch_execz .LBB0_624
	s_andn2_b64 vcc, exec, s[4:5]
	s_cbranch_vccnz .LBB0_623
	ds_read2st64_b32 v[18:19], v168 offset1:2
	ds_read2st64_b32 v[20:21], v168 offset0:4 offset1:6
	ds_read2st64_b32 v[22:23], v168 offset0:8 offset1:10
	ds_read2st64_b32 v[24:25], v168 offset0:28 offset1:30
	ds_read2st64_b32 v[26:27], v168 offset0:24 offset1:26
	ds_read2st64_b32 v[28:29], v168 offset0:20 offset1:22
	ds_read2st64_b32 v[30:31], v168 offset0:16 offset1:18
	ds_read2st64_b32 v[32:33], v168 offset0:12 offset1:14
	s_waitcnt lgkmcnt(4)
	v_pk_add_f32 v[16:17], v[16:17], v[24:25]
	s_waitcnt lgkmcnt(3)
	v_pk_add_f32 v[14:15], v[14:15], v[26:27]
	s_waitcnt lgkmcnt(2)
	v_pk_add_f32 v[12:13], v[12:13], v[28:29]
	s_waitcnt lgkmcnt(1)
	v_pk_add_f32 v[10:11], v[10:11], v[30:31]
	s_waitcnt lgkmcnt(0)
	v_pk_add_f32 v[8:9], v[8:9], v[32:33]
	v_pk_add_f32 v[6:7], v[6:7], v[22:23]
	v_pk_add_f32 v[4:5], v[4:5], v[20:21]
	v_pk_add_f32 v[2:3], v[2:3], v[18:19]
	s_branch .LBB0_623
